# alignment-barrier deferral extended to P3, P4 and P6 (the leading wave group's unit-scheduling code runs under the other group's last MFMA interval in every GEMM phase)
# baseline (speedup 1.0000x reference)
; #define PG8_STAGE(bufoff, gbase, voff) do { PG8_GLDS((const char*)(gbase), (voff)[0], ldsb + (bufoff)); PG8_GLDS((const char*)(gbase), (voff)[1], ldsb + (bufoff) + 8192u); } while (0)
; #define PG8_WAIT_VR() PG8_WAIT_V(8)
; #define PG8_WAIT_L(n) asm volatile("s_waitcnt lgkmcnt(" #n ")" ::: "memory")
; template <class Epi, class Sched, bool F8 = false, bool PF = false, bool I8 = false, int PID = -1>
; __device__ __forceinline__ void gemm_phase(LAS unsigned char* lds, LAS unsigned char* xlds, const int RP, const int RPB, const int nt, const Sched& S, const Epi& E, const int stagger_ticks) {
;     ...
;         for (int t = 0; t < nt; t += 2) {
;             const bool last = (t == nt - 2);
;             unsigned ldsb = ldsb0; asm volatile("" : "+s"(ldsb));
;             const char* a1 = cA + (size_t)(t + 1) * kstep;
;             const char* a2 = last ? nA : cA + (size_t)(t + 2) * kstep; const char* b2 = last ? nB : cB + (size_t)(t + 2) * kstep;
;             const char* a3 = a2 + kstep; const char* b3 = b2 + kstep;
;             if constexpr (PF) { const char* pfa = (t + 4 < nt) ? cA + (size_t)(t + 4) * kstep : nA + (size_t)(t + 4 - nt) * kstep;
;                 asm volatile("s_mov_b32 m0, %2\n\ts_nop 0\n\tglobal_load_lds_dword %0, %1" :: "v"(voffP), "s"(pfa), "s"(ldsP) : "memory", "m0"); }
;             const bool relax = (Epi::RELAX > 0) && (t == 0) && epi_ran;
;             PG8_LDB(B0, 0, 0); PG8_LDB(B1, 0, 1); PG8_SCHED; PG8_LDA(At, 0, 0); PG8_STAGEA1(PG8_SA(1, 1), a1);
;             if (Sched::GATHER) { if (last) { const u32x4 nv = *nslot; vA0 = nv.x; vA1 = nv.y; vA2 = nv.z; vA3 = nv.w; } }
;             PG8_WAIT_VX(); PG8_WAIT_L(0); PG8_BAR; PG8_MMA(0, 0, At, B0); PG8_MMA(0, 1, At, B1); PG8_BAR; PG8_SCHED;
;             if constexpr (Epi::BIAS_DMA) { if (t == 0 && has_next) E.bias_dma(nxt, xlds + 8192 + ((ui + 1) & 1) * Epi::BIAS_STRIDE, wid, lane); }
;             PG8_LDA(At, 0, 1); PG8_STAGE(PG8_SB(0, 0), b2, voffB); PG8_STAGE(PG8_SB(0, 1), b2 + hstepB, voffB); PG8_STAGEA(PG8_SA(0, 0), a2, vA0, vA1);
;             PG8_WAIT_VX(); PG8_WAIT_L(0); PG8_BAR; PG8_MMA(1, 0, At, B0); PG8_MMA(1, 1, At, B1); PG8_BAR; PG8_SCHED;
;             PG8_LDB(B0, 1, 0); PG8_LDB(B1, 1, 1); PG8_SCHED; PG8_LDA(At, 1, 0); PG8_STAGEA1(PG8_SA(0, 1), a2);
;             PG8_WAIT_VR(); PG8_WAIT_L(0); PG8_BAR; PG8_MMA(0, 0, At, B0); PG8_MMA(0, 1, At, B1); PG8_BAR; PG8_SCHED;
.LBB0_547:
	s_mov_b32 s47, s5
	s_add_u32 s100, s0, 0xfffc0000
	s_addc_u32 s101, s1, -1
	s_add_i32 s48, s47, 0x8000
	s_mov_b32 m0, s48
	s_nop 0
	global_load_lds_dwordx4 v1, s[100:101]
	s_add_i32 s48, s47, 0xa000
	s_mov_b32 m0, s48
	s_nop 0
	global_load_lds_dwordx4 v192, s[100:101]
	v_add_u32_e32 v142, 0x10000, v195
	v_add_u32_e32 v158, 0x14000, v195
	ds_read_b128 v[130:133], v142
	ds_read_b128 v[134:137], v142 offset:1024
	ds_read_b128 v[138:141], v142 offset:2048
	ds_read_b128 v[142:145], v142 offset:3072
	ds_read_b128 v[146:149], v158
	ds_read_b128 v[150:153], v158 offset:1024
	ds_read_b128 v[154:157], v158 offset:2048
	ds_read_b128 v[158:161], v158 offset:3072
	s_add_u32 s2, s0, 0xfffc0080
	s_addc_u32 s3, s1, -1
	s_cmp_eq_u32 s46, 12
	s_cselect_b32 s36, s8, s2
	s_cselect_b32 s37, s9, s3
	s_cselect_b32 s34, s10, s20
	s_cselect_b32 s35, s11, s45
	s_add_u32 s2, s36, 0x80
	s_addc_u32 s3, s37, 0
	ds_read_b128 v[162:165], v196
	ds_read_b128 v[166:169], v196 offset:1024
	ds_read_b128 v[170:173], v196 offset:2048
	ds_read_b128 v[174:177], v196 offset:3072
	ds_read_b128 v[180:183], v196 offset:4096
	ds_read_b128 v[184:187], v196 offset:5120
	ds_read_b128 v[188:191], v196 offset:6144
	ds_read_b128 v[198:201], v196 offset:7168
	s_add_i32 s48, s47, 0xc000
	s_mov_b32 m0, s48
	s_nop 0
	global_load_lds_dwordx4 v1, s[0:1]
	s_add_i32 s48, s47, 0xe000
	s_mov_b32 m0, s48
	s_nop 0
	global_load_lds_dwordx4 v192, s[0:1]
	s_waitcnt vmcnt(8)
	s_waitcnt lgkmcnt(0)
	s_barrier
	s_setprio 1
	s_waitcnt lgkmcnt(7)
	v_mfma_f32_16x16x32_bf16 v[114:117], v[130:133], v[162:165], v[114:117]
	v_mfma_f32_16x16x32_bf16 v[118:121], v[138:141], v[162:165], v[118:121]
	s_waitcnt lgkmcnt(5)
	v_mfma_f32_16x16x32_bf16 v[110:113], v[130:133], v[170:173], v[110:113]
	v_mfma_f32_16x16x32_bf16 v[106:109], v[138:141], v[170:173], v[106:109]
	s_waitcnt lgkmcnt(3)
	v_mfma_f32_16x16x32_bf16 v[94:97], v[130:133], v[180:183], v[94:97]
	v_mfma_f32_16x16x32_bf16 v[90:93], v[138:141], v[180:183], v[90:93]
	s_waitcnt lgkmcnt(1)
	v_mfma_f32_16x16x32_bf16 v[78:81], v[130:133], v[188:191], v[78:81]
	v_mfma_f32_16x16x32_bf16 v[74:77], v[138:141], v[188:191], v[74:77]
	v_mfma_f32_16x16x32_bf16 v[114:117], v[134:137], v[166:169], v[114:117]
	v_mfma_f32_16x16x32_bf16 v[118:121], v[142:145], v[166:169], v[118:121]
	v_mfma_f32_16x16x32_bf16 v[110:113], v[134:137], v[174:177], v[110:113]
	v_mfma_f32_16x16x32_bf16 v[106:109], v[142:145], v[174:177], v[106:109]
	v_mfma_f32_16x16x32_bf16 v[94:97], v[134:137], v[184:187], v[94:97]
	v_mfma_f32_16x16x32_bf16 v[90:93], v[142:145], v[184:187], v[90:93]
	s_waitcnt lgkmcnt(0)
	v_mfma_f32_16x16x32_bf16 v[78:81], v[134:137], v[198:201], v[78:81]
	v_mfma_f32_16x16x32_bf16 v[74:77], v[142:145], v[198:201], v[74:77]
	v_mfma_f32_16x16x32_bf16 v[126:129], v[146:149], v[162:165], v[126:129]
	v_mfma_f32_16x16x32_bf16 v[122:125], v[154:157], v[162:165], v[122:125]
	v_mfma_f32_16x16x32_bf16 v[102:105], v[146:149], v[170:173], v[102:105]
	v_mfma_f32_16x16x32_bf16 v[98:101], v[154:157], v[170:173], v[98:101]
	v_mfma_f32_16x16x32_bf16 v[86:89], v[146:149], v[180:183], v[86:89]
	v_mfma_f32_16x16x32_bf16 v[82:85], v[154:157], v[180:183], v[82:85]
	v_mfma_f32_16x16x32_bf16 v[70:73], v[146:149], v[188:191], v[70:73]
	v_mfma_f32_16x16x32_bf16 v[66:69], v[154:157], v[188:191], v[66:69]
	v_mfma_f32_16x16x32_bf16 v[126:129], v[150:153], v[166:169], v[126:129]
	v_mfma_f32_16x16x32_bf16 v[122:125], v[158:161], v[166:169], v[122:125]
	v_mfma_f32_16x16x32_bf16 v[102:105], v[150:153], v[174:177], v[102:105]
	v_mfma_f32_16x16x32_bf16 v[98:101], v[158:161], v[174:177], v[98:101]
	v_mfma_f32_16x16x32_bf16 v[86:89], v[150:153], v[184:187], v[86:89]
	v_mfma_f32_16x16x32_bf16 v[82:85], v[158:161], v[184:187], v[82:85]
	v_mfma_f32_16x16x32_bf16 v[70:73], v[150:153], v[198:201], v[70:73]
	v_mfma_f32_16x16x32_bf16 v[66:69], v[158:161], v[198:201], v[66:69]
	s_setprio 0
	s_barrier
	ds_read_b128 v[162:165], v196 offset:16384
	ds_read_b128 v[166:169], v196 offset:17408
	ds_read_b128 v[170:173], v196 offset:18432
	ds_read_b128 v[174:177], v196 offset:19456
	ds_read_b128 v[180:183], v196 offset:20480
	ds_read_b128 v[184:187], v196 offset:21504
	ds_read_b128 v[188:191], v196 offset:22528
	ds_read_b128 v[198:201], v196 offset:23552
	s_add_i32 s48, s47, 0x10000
	s_mov_b32 m0, s48
	s_nop 0
	global_load_lds_dwordx4 v193, s[34:35]
	s_add_i32 s48, s47, 0x12000
	s_mov_b32 m0, s48
	s_nop 0
	global_load_lds_dwordx4 v194, s[34:35]
	s_add_u32 s48, s34, 0x4000
	s_addc_u32 s49, s35, 0
	s_add_i32 s50, s47, 0x14000
	s_mov_b32 m0, s50
	s_nop 0
	global_load_lds_dwordx4 v193, s[48:49]
	s_add_i32 s50, s47, 0x16000
	s_mov_b32 m0, s50
	s_nop 0
	global_load_lds_dwordx4 v194, s[48:49]
	s_waitcnt vmcnt(6)
	s_waitcnt lgkmcnt(0)
	s_barrier
; #define PG8_STAGE(bufoff, gbase, voff) do { PG8_GLDS((const char*)(gbase), (voff)[0], ldsb + (bufoff)); PG8_GLDS((const char*)(gbase), (voff)[1], ldsb + (bufoff) + 8192u); } while (0)
; #define PG8_STAGEA(bufoff, gbase, o0, o1) do { PG8_GLDS((const char*)(gbase), (o0), ldsb + (bufoff)); PG8_GLDS((const char*)(gbase), (o1), ldsb + (bufoff) + 8192u); } while (0)
; #define PG8_STAGEA1(bufoff, gbase) do { if constexpr (Sched::GATHER) { PG8_STAGEA(bufoff, gbase, vA2, vA3); } else { PG8_STAGEA(bufoff, (gbase) + hstep, vA0, vA1); } } while (0)
; #define PG8_LDA(dst, b, h) do { if constexpr (F8) { _Pragma("unroll") for (int m = 0; m < 4; ++m) dst##8[m] = PG8_LD32(lds + PG8_SA(b, h) + aoff + m * 2048); } else { \
;         _Pragma("unroll") for (int m = 0; m < 4; ++m) _Pragma("unroll") for (int k = 0; k < 2; ++k) dst[m][k] = *(const LAS bf16x8*)(lds + PG8_SA(b, h) + aoff + m * 2048 + k * 1024); } } while (0)
; #define PG8_LDB(dst, b, h) do { if constexpr (F8) { _Pragma("unroll") for (int n = 0; n < 2; ++n) dst##8[n] = PG8_LD32(lds + PG8_SB(b, h) + boff + n * 2048); } else { \
;         _Pragma("unroll") for (int n = 0; n < 2; ++n) _Pragma("unroll") for (int k = 0; k < 2; ++k) dst[n][k] = *(const LAS bf16x8*)(lds + PG8_SB(b, h) + boff + n * 2048 + k * 1024); } } while (0)
; #define PG8_WAIT_VR() PG8_WAIT_V(8)
; template <class Epi, class Sched, bool F8 = false, bool PF = false, bool I8 = false, int PID = -1>
; __device__ __forceinline__ void gemm_phase(LAS unsigned char* lds, LAS unsigned char* xlds, const int RP, const int RPB, const int nt, const Sched& S, const Epi& E, const int stagger_ticks) {
;     ...
;             PG8_LDA(At, 0, 1); PG8_STAGE(PG8_SB(0, 0), b2, voffB); PG8_STAGE(PG8_SB(0, 1), b2 + hstepB, voffB); PG8_STAGEA(PG8_SA(0, 0), a2, vA0, vA1);
;             PG8_WAIT_VX(); PG8_WAIT_L(0); PG8_BAR; PG8_MMA(1, 0, At, B0); PG8_MMA(1, 1, At, B1); PG8_BAR; PG8_SCHED;
;             PG8_LDB(B0, 1, 0); PG8_LDB(B1, 1, 1); PG8_SCHED; PG8_LDA(At, 1, 0); PG8_STAGEA1(PG8_SA(0, 1), a2);
;             PG8_WAIT_VR(); PG8_WAIT_L(0); PG8_BAR; PG8_MMA(0, 0, At, B0); PG8_MMA(0, 1, At, B1); PG8_BAR; PG8_SCHED;
;             PG8_LDA(At, 1, 1); PG8_STAGE(PG8_SB(1, 0), b3, voffB); PG8_STAGE(PG8_SB(1, 1), b3 + hstepB, voffB); PG8_STAGEA(PG8_SA(1, 0), a3, vA0, vA1);
;             PG8_WAIT_VR(); PG8_WAIT_L(0); PG8_BAR; PG8_MMA(1, 0, At, B0); PG8_MMA(1, 1, At, B1); PG8_BAR; PG8_SCHED;
	s_setprio 1
	s_waitcnt lgkmcnt(7)
	v_mfma_f32_16x16x32_bf16 v[50:53], v[130:133], v[162:165], v[50:53]
	v_mfma_f32_16x16x32_bf16 v[54:57], v[138:141], v[162:165], v[54:57]
	s_waitcnt lgkmcnt(5)
	v_mfma_f32_16x16x32_bf16 v[46:49], v[130:133], v[170:173], v[46:49]
	v_mfma_f32_16x16x32_bf16 v[42:45], v[138:141], v[170:173], v[42:45]
	s_waitcnt lgkmcnt(3)
	v_mfma_f32_16x16x32_bf16 v[30:33], v[130:133], v[180:183], v[30:33]
	v_mfma_f32_16x16x32_bf16 v[26:29], v[138:141], v[180:183], v[26:29]
	s_waitcnt lgkmcnt(1)
	v_mfma_f32_16x16x32_bf16 v[14:17], v[130:133], v[188:191], v[14:17]
	v_mfma_f32_16x16x32_bf16 v[10:13], v[138:141], v[188:191], v[10:13]
	v_mfma_f32_16x16x32_bf16 v[50:53], v[134:137], v[166:169], v[50:53]
	v_mfma_f32_16x16x32_bf16 v[54:57], v[142:145], v[166:169], v[54:57]
	v_mfma_f32_16x16x32_bf16 v[46:49], v[134:137], v[174:177], v[46:49]
	v_mfma_f32_16x16x32_bf16 v[42:45], v[142:145], v[174:177], v[42:45]
	v_mfma_f32_16x16x32_bf16 v[30:33], v[134:137], v[184:187], v[30:33]
	v_mfma_f32_16x16x32_bf16 v[26:29], v[142:145], v[184:187], v[26:29]
	s_waitcnt lgkmcnt(0)
	v_mfma_f32_16x16x32_bf16 v[14:17], v[134:137], v[198:201], v[14:17]
	v_mfma_f32_16x16x32_bf16 v[10:13], v[142:145], v[198:201], v[10:13]
	v_mfma_f32_16x16x32_bf16 v[58:61], v[146:149], v[162:165], v[58:61]
	v_mfma_f32_16x16x32_bf16 v[62:65], v[154:157], v[162:165], v[62:65]
	v_mfma_f32_16x16x32_bf16 v[38:41], v[146:149], v[170:173], v[38:41]
	v_mfma_f32_16x16x32_bf16 v[34:37], v[154:157], v[170:173], v[34:37]
	v_mfma_f32_16x16x32_bf16 v[22:25], v[146:149], v[180:183], v[22:25]
	v_mfma_f32_16x16x32_bf16 v[18:21], v[154:157], v[180:183], v[18:21]
	v_mfma_f32_16x16x32_bf16 v[6:9], v[146:149], v[188:191], v[6:9]
	v_mfma_f32_16x16x32_bf16 v[2:5], v[154:157], v[188:191], v[2:5]
	v_mfma_f32_16x16x32_bf16 v[58:61], v[150:153], v[166:169], v[58:61]
	v_mfma_f32_16x16x32_bf16 v[62:65], v[158:161], v[166:169], v[62:65]
	v_mfma_f32_16x16x32_bf16 v[38:41], v[150:153], v[174:177], v[38:41]
	v_mfma_f32_16x16x32_bf16 v[34:37], v[158:161], v[174:177], v[34:37]
	v_mfma_f32_16x16x32_bf16 v[22:25], v[150:153], v[184:187], v[22:25]
	v_mfma_f32_16x16x32_bf16 v[18:21], v[158:161], v[184:187], v[18:21]
	v_mfma_f32_16x16x32_bf16 v[6:9], v[150:153], v[198:201], v[6:9]
	v_mfma_f32_16x16x32_bf16 v[2:5], v[158:161], v[198:201], v[2:5]
	s_setprio 0
	s_barrier
	s_add_i32 s48, s47, 0x2000
	s_mov_b32 m0, s47
	s_nop 0
	global_load_lds_dwordx4 v1, s[36:37]
	s_nop 0
	s_mov_b32 m0, s48
	s_nop 0
	global_load_lds_dwordx4 v192, s[36:37]
	v_add_u32_e32 v142, 0x18000, v195
	v_add_u32_e32 v158, 0x1c000, v195
	ds_read_b128 v[130:133], v142
	ds_read_b128 v[134:137], v142 offset:1024
	ds_read_b128 v[138:141], v142 offset:2048
	ds_read_b128 v[142:145], v142 offset:3072
	ds_read_b128 v[146:149], v158
	ds_read_b128 v[150:153], v158 offset:1024
	ds_read_b128 v[154:157], v158 offset:2048
	ds_read_b128 v[158:161], v158 offset:3072
	ds_read_b128 v[162:165], v196 offset:32768
	ds_read_b128 v[166:169], v196 offset:33792
	ds_read_b128 v[170:173], v196 offset:34816
	ds_read_b128 v[174:177], v196 offset:35840
	ds_read_b128 v[180:183], v196 offset:36864
	ds_read_b128 v[184:187], v196 offset:37888
	ds_read_b128 v[188:191], v196 offset:38912
	ds_read_b128 v[198:201], v196 offset:39936
	s_add_u32 s36, s36, 0x40000
	s_addc_u32 s37, s37, 0
	s_add_i32 s48, s47, 0x4000
	s_mov_b32 m0, s48
	s_nop 0
	global_load_lds_dwordx4 v1, s[36:37]
	s_add_i32 s48, s47, 0x6000
	s_mov_b32 m0, s48
	s_nop 0
	global_load_lds_dwordx4 v192, s[36:37]
	s_waitcnt vmcnt(8)
	s_waitcnt lgkmcnt(0)
	s_barrier
	s_setprio 1
	s_waitcnt lgkmcnt(7)
	v_mfma_f32_16x16x32_bf16 v[114:117], v[130:133], v[162:165], v[114:117]
	v_mfma_f32_16x16x32_bf16 v[118:121], v[138:141], v[162:165], v[118:121]
	s_waitcnt lgkmcnt(5)
	v_mfma_f32_16x16x32_bf16 v[110:113], v[130:133], v[170:173], v[110:113]
	v_mfma_f32_16x16x32_bf16 v[106:109], v[138:141], v[170:173], v[106:109]
	s_waitcnt lgkmcnt(3)
	v_mfma_f32_16x16x32_bf16 v[94:97], v[130:133], v[180:183], v[94:97]
	v_mfma_f32_16x16x32_bf16 v[90:93], v[138:141], v[180:183], v[90:93]
	s_waitcnt lgkmcnt(1)
	v_mfma_f32_16x16x32_bf16 v[78:81], v[130:133], v[188:191], v[78:81]
	v_mfma_f32_16x16x32_bf16 v[74:77], v[138:141], v[188:191], v[74:77]
	v_mfma_f32_16x16x32_bf16 v[114:117], v[134:137], v[166:169], v[114:117]
	v_mfma_f32_16x16x32_bf16 v[118:121], v[142:145], v[166:169], v[118:121]
	v_mfma_f32_16x16x32_bf16 v[110:113], v[134:137], v[174:177], v[110:113]
	v_mfma_f32_16x16x32_bf16 v[106:109], v[142:145], v[174:177], v[106:109]
	v_mfma_f32_16x16x32_bf16 v[94:97], v[134:137], v[184:187], v[94:97]
	v_mfma_f32_16x16x32_bf16 v[90:93], v[142:145], v[184:187], v[90:93]
	s_waitcnt lgkmcnt(0)
	v_mfma_f32_16x16x32_bf16 v[78:81], v[134:137], v[198:201], v[78:81]
	v_mfma_f32_16x16x32_bf16 v[74:77], v[142:145], v[198:201], v[74:77]
	v_mfma_f32_16x16x32_bf16 v[126:129], v[146:149], v[162:165], v[126:129]
	v_mfma_f32_16x16x32_bf16 v[122:125], v[154:157], v[162:165], v[122:125]
	v_mfma_f32_16x16x32_bf16 v[102:105], v[146:149], v[170:173], v[102:105]
	v_mfma_f32_16x16x32_bf16 v[98:101], v[154:157], v[170:173], v[98:101]
	v_mfma_f32_16x16x32_bf16 v[86:89], v[146:149], v[180:183], v[86:89]
	v_mfma_f32_16x16x32_bf16 v[82:85], v[154:157], v[180:183], v[82:85]
	v_mfma_f32_16x16x32_bf16 v[70:73], v[146:149], v[188:191], v[70:73]
	v_mfma_f32_16x16x32_bf16 v[66:69], v[154:157], v[188:191], v[66:69]
	v_mfma_f32_16x16x32_bf16 v[126:129], v[150:153], v[166:169], v[126:129]
	v_mfma_f32_16x16x32_bf16 v[122:125], v[158:161], v[166:169], v[122:125]
	v_mfma_f32_16x16x32_bf16 v[102:105], v[150:153], v[174:177], v[102:105]
	v_mfma_f32_16x16x32_bf16 v[98:101], v[158:161], v[174:177], v[98:101]
	v_mfma_f32_16x16x32_bf16 v[86:89], v[150:153], v[184:187], v[86:89]
	v_mfma_f32_16x16x32_bf16 v[82:85], v[158:161], v[184:187], v[82:85]
	v_mfma_f32_16x16x32_bf16 v[70:73], v[150:153], v[198:201], v[70:73]
	v_mfma_f32_16x16x32_bf16 v[66:69], v[158:161], v[198:201], v[66:69]
	s_setprio 0
	s_barrier
; #define PG8_WAIT_VR() PG8_WAIT_V(8)
; #define PG8_WAIT_L(n) asm volatile("s_waitcnt lgkmcnt(" #n ")" ::: "memory")
; #define PG8_BAR __builtin_amdgcn_s_barrier()
; #define PG8_SCHED __builtin_amdgcn_sched_barrier(0)
; #define PROF_BEGIN(sel) do { if constexpr (PROF && PROF_SEL == (sel)) prof_t0 = (unsigned)__builtin_amdgcn_s_memrealtime(); } while (0)
; #define PROF_END(sel) do { if constexpr (PROF && PROF_SEL == (sel)) prof_acc += (unsigned)__builtin_amdgcn_s_memrealtime() - prof_t0; } while (0)
;     __device__ __forceinline__ bool next(int i, pg8::Unit& u) const { const int L = i * G + c; if (L >= nM * 4) return false; int pm, pn; pg8::tile_remap<4>(L, nM, pm, pn); if (rev) pm = nM - 1 - pm; u.pm = pm; u.pn = pn; u.aux = 0; u.skip = 0; return true; }
;     __device__ __forceinline__ bool next(int i, pg8::Unit& u) const { const int L = first + i * stride; if (i >= nmine || L >= 512) return false; u.pm = L & 3; u.pn = (L >> 2) & 3; u.aux = L >> 4; u.skip = 0; return true; }
;     __device__ __forceinline__ bool next(int i, pg8::Unit& u) const { if (!TW) { const bool r = Base::next(i, u); u.skip = 0; return r; } const bool r = Base::next(i >> 1, u); u.skip = !(i & 1); return r; }
; template <class Epi, class Sched, bool F8 = false, bool PF = false, bool I8 = false, int PID = -1>
; __device__ __forceinline__ void gemm_phase(LAS unsigned char* lds, LAS unsigned char* xlds, const int RP, const int RPB, const int nt, const Sched& S, const Epi& E, const int stagger_ticks) {
;     ...
;             PG8_WAIT_VR(); PG8_WAIT_L(0); PG8_BAR; PG8_MMA(1, 0, At, B0); PG8_MMA(1, 1, At, B1); PG8_BAR; PG8_SCHED;
;         }
;         PROF_END(1); PROF_BEGIN(3);
;         if (wr == 0) PG8_BAR;
;         Unit nn; bool has_nn = false; unsigned gv[4] = {vA0, vA1, vA2, vA3};
;         if (has_next) { has_nn = S.next(ui + 2, nn); if (Sched::GATHER) { if (has_nn) S.a_offsets(nn, Rr, Cc, RP, gv); } }
	s_add_u32 s36, s34, 0x80
	ds_read_b128 v[162:165], v196 offset:49152
	ds_read_b128 v[166:169], v196 offset:50176
	ds_read_b128 v[170:173], v196 offset:51200
	ds_read_b128 v[174:177], v196 offset:52224
	ds_read_b128 v[180:183], v196 offset:53248
	ds_read_b128 v[184:187], v196 offset:54272
	ds_read_b128 v[188:191], v196 offset:55296
	ds_read_b128 v[198:201], v196 offset:56320
	s_addc_u32 s37, s35, 0
	s_add_i32 s48, s47, 0x18000
	s_mov_b32 m0, s48
	s_nop 0
	global_load_lds_dwordx4 v193, s[36:37]
	s_add_i32 s48, s47, 0x1a000
	s_mov_b32 m0, s48
	s_nop 0
	global_load_lds_dwordx4 v194, s[36:37]
	s_add_u32 s34, s34, 0x4080
	s_addc_u32 s35, s35, 0
	s_add_i32 s36, s47, 0x1c000
	s_mov_b32 m0, s36
	s_nop 0
	global_load_lds_dwordx4 v193, s[34:35]
	s_add_i32 s36, s47, 0x1e000
	s_mov_b32 m0, s36
	s_nop 0
	global_load_lds_dwordx4 v194, s[34:35]
	s_waitcnt vmcnt(6)
	s_waitcnt lgkmcnt(0)
	s_barrier
	s_setprio 1
	s_waitcnt lgkmcnt(7)
	v_mfma_f32_16x16x32_bf16 v[50:53], v[130:133], v[162:165], v[50:53]
	v_mfma_f32_16x16x32_bf16 v[54:57], v[138:141], v[162:165], v[54:57]
	s_waitcnt lgkmcnt(5)
	v_mfma_f32_16x16x32_bf16 v[46:49], v[130:133], v[170:173], v[46:49]
	v_mfma_f32_16x16x32_bf16 v[42:45], v[138:141], v[170:173], v[42:45]
	s_waitcnt lgkmcnt(3)
	v_mfma_f32_16x16x32_bf16 v[30:33], v[130:133], v[180:183], v[30:33]
	v_mfma_f32_16x16x32_bf16 v[26:29], v[138:141], v[180:183], v[26:29]
	s_waitcnt lgkmcnt(1)
	v_mfma_f32_16x16x32_bf16 v[14:17], v[130:133], v[188:191], v[14:17]
	v_mfma_f32_16x16x32_bf16 v[10:13], v[138:141], v[188:191], v[10:13]
	v_mfma_f32_16x16x32_bf16 v[50:53], v[134:137], v[166:169], v[50:53]
	v_mfma_f32_16x16x32_bf16 v[54:57], v[142:145], v[166:169], v[54:57]
	v_mfma_f32_16x16x32_bf16 v[46:49], v[134:137], v[174:177], v[46:49]
	v_mfma_f32_16x16x32_bf16 v[42:45], v[142:145], v[174:177], v[42:45]
	v_mfma_f32_16x16x32_bf16 v[30:33], v[134:137], v[184:187], v[30:33]
	v_mfma_f32_16x16x32_bf16 v[26:29], v[142:145], v[184:187], v[26:29]
	s_waitcnt lgkmcnt(0)
	v_mfma_f32_16x16x32_bf16 v[14:17], v[134:137], v[198:201], v[14:17]
	v_mfma_f32_16x16x32_bf16 v[10:13], v[142:145], v[198:201], v[10:13]
	v_mfma_f32_16x16x32_bf16 v[58:61], v[146:149], v[162:165], v[58:61]
	v_mfma_f32_16x16x32_bf16 v[62:65], v[154:157], v[162:165], v[62:65]
	v_mfma_f32_16x16x32_bf16 v[38:41], v[146:149], v[170:173], v[38:41]
	v_mfma_f32_16x16x32_bf16 v[34:37], v[154:157], v[170:173], v[34:37]
	v_mfma_f32_16x16x32_bf16 v[22:25], v[146:149], v[180:183], v[22:25]
	v_mfma_f32_16x16x32_bf16 v[18:21], v[154:157], v[180:183], v[18:21]
	v_mfma_f32_16x16x32_bf16 v[6:9], v[146:149], v[188:191], v[6:9]
	v_mfma_f32_16x16x32_bf16 v[2:5], v[154:157], v[188:191], v[2:5]
	v_mfma_f32_16x16x32_bf16 v[58:61], v[150:153], v[166:169], v[58:61]
	v_mfma_f32_16x16x32_bf16 v[62:65], v[158:161], v[166:169], v[62:65]
	v_mfma_f32_16x16x32_bf16 v[38:41], v[150:153], v[174:177], v[38:41]
	v_mfma_f32_16x16x32_bf16 v[34:37], v[158:161], v[174:177], v[34:37]
	v_mfma_f32_16x16x32_bf16 v[22:25], v[150:153], v[184:187], v[22:25]
	v_mfma_f32_16x16x32_bf16 v[18:21], v[158:161], v[184:187], v[18:21]
	v_mfma_f32_16x16x32_bf16 v[6:9], v[150:153], v[198:201], v[6:9]
	v_mfma_f32_16x16x32_bf16 v[2:5], v[158:161], v[198:201], v[2:5]
	s_setprio 0
	s_barrier
	s_add_i32 s46, s46, 2
	s_add_u32 s20, s20, 0x100
	s_addc_u32 s45, s45, 0
	s_add_u32 s0, s0, 0x100
	s_addc_u32 s1, s1, 0
	s_cmp_gt_u32 s46, 13
	s_cbranch_scc0 .LBB0_547
.LBB0_550:
	v_cndmask_b32_e64 v130, 0, 1, s[12:13]
	v_cmp_ne_u32_e64 s[0:1], 1, v130
	s_andn2_b64 vcc, exec, s[12:13]
	s_cbranch_vccnz .LBB0_553
	s_add_i32 s2, s44, 2
	s_mul_i32 s2, s2, s92
	s_add_i32 s2, s2, s33
	s_cmpk_gt_i32 s2, 0x3ff
	s_mov_b64 s[12:13], 0
	s_cbranch_scc1 .LBB0_554
	s_lshl_b32 s3, s2, 7
	s_and_b32 s3, s3, 0x380
	s_ashr_i32 s2, s2, 3
	s_add_i32 s2, s3, s2
	s_ashr_i32 s3, s2, 31
	s_lshr_b32 s3, s3, 27
	s_add_i32 s3, s2, s3
	s_ashr_i32 s12, s3, 5
	s_andn2_b32 s3, s3, 31
	s_sub_i32 s2, s2, s3
	s_ashr_i32 s3, s2, 31
	s_lshr_b32 s3, s3, 29
	s_add_i32 s3, s2, s3
	s_ashr_i32 s14, s3, 3
	s_and_b32 s3, s3, -8
	s_lshl_b32 s12, s12, 3
	s_sub_i32 s2, s2, s3
	s_add_i32 s12, s12, s2
	s_sub_i32 s18, 0xff, s12
	s_mov_b64 s[12:13], -1
	s_branch .LBB0_554

; __device__ __forceinline__ int opaque(int x) { asm volatile("" : "+v"(x)); return x; }
; #define PG8_BAR __builtin_amdgcn_s_barrier()
; #define PROF_BEGIN(sel) do { if constexpr (PROF && PROF_SEL == (sel)) prof_t0 = (unsigned)__builtin_amdgcn_s_memrealtime(); } while (0)
; #define PROF_END(sel) do { if constexpr (PROF && PROF_SEL == (sel)) prof_acc += (unsigned)__builtin_amdgcn_s_memrealtime() - prof_t0; } while (0)
;     __device__ __forceinline__ bool next(int i, pg8::Unit& u) const { const int L = i * G + c; if (L >= nM * 4) return false; int pm, pn; pg8::tile_remap<4>(L, nM, pm, pn); if (rev) pm = nM - 1 - pm; u.pm = pm; u.pn = pn; u.aux = 0; u.skip = 0; return true; }
;     __device__ __forceinline__ bool next(int i, pg8::Unit& u) const { const int L = first + i * stride; if (i >= nmine || L >= 512) return false; u.pm = L & 3; u.pn = (L >> 2) & 3; u.aux = L >> 4; u.skip = 0; return true; }
;     __device__ __forceinline__ bool next(int i, pg8::Unit& u) const { if (!TW) { const bool r = Base::next(i, u); u.skip = 0; return r; } const bool r = Base::next(i >> 1, u); u.skip = !(i & 1); return r; }
; template <class Epi, class Sched, bool F8 = false, bool PF = false, bool I8 = false, int PID = -1>
; __device__ __forceinline__ void gemm_phase(LAS unsigned char* lds, LAS unsigned char* xlds, const int RP, const int RPB, const int nt, const Sched& S, const Epi& E, const int stagger_ticks) {
;     ...
;         if (wr == 0) PG8_BAR;
;         Unit nn; bool has_nn = false; unsigned gv[4] = {vA0, vA1, vA2, vA3};
;         if (has_next) { has_nn = S.next(ui + 2, nn); if (Sched::GATHER) { if (has_nn) S.a_offsets(nn, Rr, Cc, RP, gv); } }
;         cur.par = ui & 1;
;         PROF_END(3); PROF_BEGIN(2);
;         if (!cur.skip) { const int t2 = opaque((int)threadIdx.x), fr2 = t2 & 15, fq2 = (t2 >> 4) & 3; E(acc, cur, wr, wc, fr2, fq2); }
.LBB0_554:
	s_and_b64 vcc, exec, s[30:31]
	s_cbranch_vccz .Lmy_nobar3
	s_barrier

; #define PG8_STAGE(bufoff, gbase, voff) do { PG8_GLDS((const char*)(gbase), (voff)[0], ldsb + (bufoff)); PG8_GLDS((const char*)(gbase), (voff)[1], ldsb + (bufoff) + 8192u); } while (0)
; #define PG8_STAGEA(bufoff, gbase, o0, o1) do { PG8_GLDS((const char*)(gbase), (o0), ldsb + (bufoff)); PG8_GLDS((const char*)(gbase), (o1), ldsb + (bufoff) + 8192u); } while (0)
; #define PG8_STAGEA1(bufoff, gbase) do { if constexpr (Sched::GATHER) { PG8_STAGEA(bufoff, gbase, vA2, vA3); } else { PG8_STAGEA(bufoff, (gbase) + hstep, vA0, vA1); } } while (0)
; #define PG8_LDA(dst, b, h) do { if constexpr (F8) { _Pragma("unroll") for (int m = 0; m < 4; ++m) dst##8[m] = PG8_LD32(lds + PG8_SA(b, h) + aoff + m * 2048); } else { \
;         _Pragma("unroll") for (int m = 0; m < 4; ++m) _Pragma("unroll") for (int k = 0; k < 2; ++k) dst[m][k] = *(const LAS bf16x8*)(lds + PG8_SA(b, h) + aoff + m * 2048 + k * 1024); } } while (0)
; #define PG8_LDB(dst, b, h) do { if constexpr (F8) { _Pragma("unroll") for (int n = 0; n < 2; ++n) dst##8[n] = PG8_LD32(lds + PG8_SB(b, h) + boff + n * 2048); } else { \
;         _Pragma("unroll") for (int n = 0; n < 2; ++n) _Pragma("unroll") for (int k = 0; k < 2; ++k) dst[n][k] = *(const LAS bf16x8*)(lds + PG8_SB(b, h) + boff + n * 2048 + k * 1024); } } while (0)
; template <class Epi, class Sched, bool F8 = false, bool PF = false, bool I8 = false, int PID = -1>
; __device__ __forceinline__ void gemm_phase(LAS unsigned char* lds, LAS unsigned char* xlds, const int RP, const int RPB, const int nt, const Sched& S, const Epi& E, const int stagger_ticks) {
;     ...
;             PG8_LDB(B0, 0, 0); PG8_LDB(B1, 0, 1); PG8_SCHED; PG8_LDA(At, 0, 0); PG8_STAGEA1(PG8_SA(1, 1), a1);
;             if (Sched::GATHER) { if (last) { const u32x4 nv = *nslot; vA0 = nv.x; vA1 = nv.y; vA2 = nv.z; vA3 = nv.w; } }
;             PG8_WAIT_VX(); PG8_WAIT_L(0); PG8_BAR; PG8_MMA(0, 0, At, B0); PG8_MMA(0, 1, At, B1); PG8_BAR; PG8_SCHED;
;             if constexpr (Epi::BIAS_DMA) { if (t == 0 && has_next) E.bias_dma(nxt, xlds + 8192 + ((ui + 1) & 1) * Epi::BIAS_STRIDE, wid, lane); }
;             PG8_LDA(At, 0, 1); PG8_STAGE(PG8_SB(0, 0), b2, voffB); PG8_STAGE(PG8_SB(0, 1), b2 + hstepB, voffB); PG8_STAGEA(PG8_SA(0, 0), a2, vA0, vA1);
;             PG8_WAIT_VX(); PG8_WAIT_L(0); PG8_BAR; PG8_MMA(1, 0, At, B0); PG8_MMA(1, 1, At, B1); PG8_BAR; PG8_SCHED;
.LBB0_641:
	s_mov_b32 s45, s29
	s_add_u32 s100, s0, 0xfffe0000
	s_addc_u32 s101, s1, -1
	s_add_i32 s46, s45, 0x8000
	s_mov_b32 m0, s46
	s_nop 0
	global_load_lds_dwordx4 v1, s[100:101]
	s_add_i32 s46, s45, 0xa000
	s_mov_b32 m0, s46
	s_nop 0
	global_load_lds_dwordx4 v194, s[100:101]
	v_add_u32_e32 v131, 0x10000, v197
	ds_read_b128 v[132:135], v131
	ds_read_b128 v[136:139], v131 offset:1024
	ds_read_b128 v[140:143], v131 offset:2048
	ds_read_b128 v[144:147], v131 offset:3072
	v_add_u32_e32 v131, 0x14000, v197
	ds_read_b128 v[148:151], v131
	ds_read_b128 v[152:155], v131 offset:1024
	ds_read_b128 v[156:159], v131 offset:2048
	ds_read_b128 v[160:163], v131 offset:3072
	s_add_u32 s2, s0, 0xfffe0080
	s_addc_u32 s3, s1, -1
	s_cmp_eq_u32 s44, 4
	s_cselect_b32 s24, s8, s2
	s_cselect_b32 s25, s9, s3
	s_cselect_b32 s4, s10, s42
	s_cselect_b32 s5, s11, s43
	s_add_u32 s2, s24, 0x80
	s_addc_u32 s3, s25, 0
	ds_read_b128 v[164:167], v198
	ds_read_b128 v[168:171], v198 offset:1024
	ds_read_b128 v[172:175], v198 offset:2048
	ds_read_b128 v[176:179], v198 offset:3072
	ds_read_b128 v[180:183], v198 offset:4096
	ds_read_b128 v[184:187], v198 offset:5120
	ds_read_b128 v[202:205], v198 offset:6144
	ds_read_b128 v[206:209], v198 offset:7168
	s_add_i32 s46, s45, 0xc000
	s_mov_b32 m0, s46
	s_nop 0
	global_load_lds_dwordx4 v1, s[0:1]
	s_add_i32 s46, s45, 0xe000
	s_mov_b32 m0, s46
	s_nop 0
	global_load_lds_dwordx4 v194, s[0:1]
	s_waitcnt vmcnt(8)
	s_waitcnt lgkmcnt(0)
	s_barrier
	s_setprio 1
	s_waitcnt lgkmcnt(6)
	v_mfma_f32_16x16x128_f8f6f4 v[114:117], v[132:139], v[164:171], v[114:117]
	v_mfma_f32_16x16x128_f8f6f4 v[118:121], v[140:147], v[164:171], v[118:121]
	s_waitcnt lgkmcnt(4)
	v_mfma_f32_16x16x128_f8f6f4 v[102:105], v[132:139], v[172:179], v[102:105]
	v_mfma_f32_16x16x128_f8f6f4 v[98:101], v[140:147], v[172:179], v[98:101]
	s_waitcnt lgkmcnt(2)
	v_mfma_f32_16x16x128_f8f6f4 v[188:191], v[132:139], v[180:187], v[86:89]
	v_mfma_f32_16x16x128_f8f6f4 v[210:213], v[140:147], v[180:187], v[82:85]
	s_waitcnt lgkmcnt(0)
	v_mfma_f32_16x16x128_f8f6f4 v[214:217], v[132:139], v[202:209], v[70:73]
	v_mfma_f32_16x16x128_f8f6f4 v[218:221], v[140:147], v[202:209], v[66:69]
	v_mfma_f32_16x16x128_f8f6f4 v[122:125], v[148:155], v[164:171], v[122:125]
	v_mfma_f32_16x16x128_f8f6f4 v[126:129], v[156:163], v[164:171], v[126:129]
	v_mfma_f32_16x16x128_f8f6f4 v[110:113], v[148:155], v[172:179], v[110:113]
	v_mfma_f32_16x16x128_f8f6f4 v[106:109], v[156:163], v[172:179], v[106:109]
	v_mfma_f32_16x16x128_f8f6f4 v[164:167], v[148:155], v[180:187], v[94:97]
	v_mfma_f32_16x16x128_f8f6f4 v[168:171], v[156:163], v[180:187], v[90:93]
	v_mfma_f32_16x16x128_f8f6f4 v[172:175], v[148:155], v[202:209], v[78:81]
	v_mfma_f32_16x16x128_f8f6f4 v[176:179], v[156:163], v[202:209], v[74:77]
	s_setprio 0
	s_barrier
	ds_read_b128 v[66:69], v198 offset:16384
	ds_read_b128 v[70:73], v198 offset:17408
	s_nop 2
	ds_read_b128 v[74:77], v198 offset:18432
	ds_read_b128 v[78:81], v198 offset:19456
	ds_read_b128 v[82:85], v198 offset:20480
	ds_read_b128 v[86:89], v198 offset:21504
	ds_read_b128 v[90:93], v198 offset:22528
	ds_read_b128 v[94:97], v198 offset:23552
	s_add_i32 s46, s45, 0x10000
	s_mov_b32 m0, s46
	s_nop 0
	global_load_lds_dwordx4 v195, s[4:5]
	s_add_i32 s46, s45, 0x12000
	s_mov_b32 m0, s46
	s_nop 0
	global_load_lds_dwordx4 v196, s[4:5]
	s_add_u32 s46, s4, 0x2000
	s_addc_u32 s47, s5, 0
	s_add_i32 s48, s45, 0x14000
	s_mov_b32 m0, s48
	s_nop 0
	global_load_lds_dwordx4 v195, s[46:47]
	s_add_i32 s48, s45, 0x16000
	s_mov_b32 m0, s48
	s_nop 0
	global_load_lds_dwordx4 v196, s[46:47]
	s_waitcnt vmcnt(6)
	s_waitcnt lgkmcnt(0)
	s_barrier
	s_setprio 1
	s_waitcnt lgkmcnt(6)
	v_mfma_f32_16x16x128_f8f6f4 v[54:57], v[132:139], v[66:73], v[54:57]
	v_mfma_f32_16x16x128_f8f6f4 v[50:53], v[140:147], v[66:73], v[50:53]
	s_waitcnt lgkmcnt(4)
	v_mfma_f32_16x16x128_f8f6f4 v[180:183], v[132:139], v[74:81], v[38:41]
	v_mfma_f32_16x16x128_f8f6f4 v[184:187], v[140:147], v[74:81], v[34:37]
	s_waitcnt lgkmcnt(2)
	v_mfma_f32_16x16x128_f8f6f4 v[202:205], v[132:139], v[82:89], v[22:25]
	v_mfma_f32_16x16x128_f8f6f4 v[206:209], v[140:147], v[82:89], v[18:21]
	s_waitcnt lgkmcnt(0)
	v_mfma_f32_16x16x128_f8f6f4 v[222:225], v[132:139], v[90:97], v[6:9]
	v_mfma_f32_16x16x128_f8f6f4 v[226:229], v[140:147], v[90:97], v[2:5]
	v_mfma_f32_16x16x128_f8f6f4 v[62:65], v[148:155], v[66:73], v[62:65]
	v_mfma_f32_16x16x128_f8f6f4 v[58:61], v[156:163], v[66:73], v[58:61]
	v_mfma_f32_16x16x128_f8f6f4 v[230:233], v[148:155], v[74:81], v[46:49]
	v_mfma_f32_16x16x128_f8f6f4 v[234:237], v[156:163], v[74:81], v[42:45]
	v_mfma_f32_16x16x128_f8f6f4 v[238:241], v[148:155], v[82:89], v[30:33]
	v_mfma_f32_16x16x128_f8f6f4 v[242:245], v[156:163], v[82:89], v[26:29]
	v_mfma_f32_16x16x128_f8f6f4 v[246:249], v[148:155], v[90:97], v[14:17]
	v_mfma_f32_16x16x128_f8f6f4 v[250:253], v[156:163], v[90:97], v[10:13]
	s_setprio 0
	s_barrier
; #define PG8_STAGE(bufoff, gbase, voff) do { PG8_GLDS((const char*)(gbase), (voff)[0], ldsb + (bufoff)); PG8_GLDS((const char*)(gbase), (voff)[1], ldsb + (bufoff) + 8192u); } while (0)
; #define PG8_STAGEA(bufoff, gbase, o0, o1) do { PG8_GLDS((const char*)(gbase), (o0), ldsb + (bufoff)); PG8_GLDS((const char*)(gbase), (o1), ldsb + (bufoff) + 8192u); } while (0)
; #define PG8_STAGEA1(bufoff, gbase) do { if constexpr (Sched::GATHER) { PG8_STAGEA(bufoff, gbase, vA2, vA3); } else { PG8_STAGEA(bufoff, (gbase) + hstep, vA0, vA1); } } while (0)
; #define PG8_WAIT_VR() PG8_WAIT_V(8)
; #define PG8_WAIT_L(n) asm volatile("s_waitcnt lgkmcnt(" #n ")" ::: "memory")
; #define PG8_BAR __builtin_amdgcn_s_barrier()
; #define PG8_SCHED __builtin_amdgcn_sched_barrier(0)
;     const int nwg = nM * NN; int wgid = L;
;     { const int q = nwg >> 3, r = nwg & 7, xcd = wgid & 7, off = wgid >> 3; wgid = (xcd < r ? xcd * (q + 1) : r * (q + 1) + (xcd - r) * q) + off; }
;     constexpr int nig = WGM * NN; const int gid = wgid / nig, idx = wgid - gid * nig, fm = gid * WGM, left = nM - fm;
;     if (left >= WGM) { pm = fm + (idx % WGM); pn = idx / WGM; } else { pm = fm + (idx % left); pn = idx / left; }
; }
; template <class Epi, class Sched, bool F8 = false, bool PF = false, bool I8 = false, int PID = -1>
; __device__ __forceinline__ void gemm_phase(LAS unsigned char* lds, LAS unsigned char* xlds, const int RP, const int RPB, const int nt, const Sched& S, const Epi& E, const int stagger_ticks) {
;     ...
;             PG8_LDB(B0, 1, 0); PG8_LDB(B1, 1, 1); PG8_SCHED; PG8_LDA(At, 1, 0); PG8_STAGEA1(PG8_SA(0, 1), a2);
;             PG8_WAIT_VR(); PG8_WAIT_L(0); PG8_BAR; PG8_MMA(0, 0, At, B0); PG8_MMA(0, 1, At, B1); PG8_BAR; PG8_SCHED;
;             PG8_LDA(At, 1, 1); PG8_STAGE(PG8_SB(1, 0), b3, voffB); PG8_STAGE(PG8_SB(1, 1), b3 + hstepB, voffB); PG8_STAGEA(PG8_SA(1, 0), a3, vA0, vA1);
;             PG8_WAIT_VR(); PG8_WAIT_L(0); PG8_BAR; PG8_MMA(1, 0, At, B0); PG8_MMA(1, 1, At, B1); PG8_BAR; PG8_SCHED;
;         }
;         PROF_END(1); PROF_BEGIN(3);
;         if (wr == 0) PG8_BAR;
;         Unit nn; bool has_nn = false; unsigned gv[4] = {vA0, vA1, vA2, vA3};
;         if (has_next) { has_nn = S.next(ui + 2, nn); if (Sched::GATHER) { if (has_nn) S.a_offsets(nn, Rr, Cc, RP, gv); } }
	s_add_i32 s46, s45, 0x2000
	s_mov_b32 m0, s45
	s_nop 0
	global_load_lds_dwordx4 v1, s[24:25]
	s_nop 0
	s_mov_b32 m0, s46
	s_nop 0
	global_load_lds_dwordx4 v194, s[24:25]
	s_nop 3
	v_add_u32_e32 v14, 0x18000, v197
	v_add_u32_e32 v18, 0x1c000, v197
	ds_read_b128 v[2:5], v14
	ds_read_b128 v[6:9], v14 offset:1024
	ds_read_b128 v[10:13], v14 offset:2048
	ds_read_b128 v[14:17], v14 offset:3072
	ds_read_b128 v[132:135], v18
	ds_read_b128 v[136:139], v18 offset:1024
	ds_read_b128 v[140:143], v18 offset:2048
	ds_read_b128 v[144:147], v18 offset:3072
	ds_read_b128 v[18:21], v198 offset:32768
	ds_read_b128 v[22:25], v198 offset:33792
	ds_read_b128 v[26:29], v198 offset:34816
	ds_read_b128 v[30:33], v198 offset:35840
	ds_read_b128 v[34:37], v198 offset:36864
	ds_read_b128 v[38:41], v198 offset:37888
	ds_read_b128 v[42:45], v198 offset:38912
	ds_read_b128 v[46:49], v198 offset:39936
	s_add_u32 s24, s24, 0x20000
	s_addc_u32 s25, s25, 0
	s_add_i32 s46, s45, 0x4000
	s_mov_b32 m0, s46
	s_nop 0
	global_load_lds_dwordx4 v1, s[24:25]
	s_add_i32 s46, s45, 0x6000
	s_mov_b32 m0, s46
	s_nop 0
	global_load_lds_dwordx4 v194, s[24:25]
	s_waitcnt vmcnt(8)
	s_waitcnt lgkmcnt(0)
	s_barrier
	s_setprio 1
	s_waitcnt lgkmcnt(6)
	v_mfma_f32_16x16x128_f8f6f4 v[114:117], v[2:9], v[18:25], v[114:117]
	v_mfma_f32_16x16x128_f8f6f4 v[118:121], v[10:17], v[18:25], v[118:121]
	s_waitcnt lgkmcnt(4)
	v_mfma_f32_16x16x128_f8f6f4 v[102:105], v[2:9], v[26:33], v[102:105]
	v_mfma_f32_16x16x128_f8f6f4 v[98:101], v[10:17], v[26:33], v[98:101]
	s_waitcnt lgkmcnt(2)
	v_mfma_f32_16x16x128_f8f6f4 v[86:89], v[2:9], v[34:41], v[188:191]
	v_mfma_f32_16x16x128_f8f6f4 v[82:85], v[10:17], v[34:41], v[210:213]
	s_waitcnt lgkmcnt(0)
	v_mfma_f32_16x16x128_f8f6f4 v[70:73], v[2:9], v[42:49], v[214:217]
	v_mfma_f32_16x16x128_f8f6f4 v[66:69], v[10:17], v[42:49], v[218:221]
	v_mfma_f32_16x16x128_f8f6f4 v[122:125], v[132:139], v[18:25], v[122:125]
	v_mfma_f32_16x16x128_f8f6f4 v[126:129], v[140:147], v[18:25], v[126:129]
	v_mfma_f32_16x16x128_f8f6f4 v[110:113], v[132:139], v[26:33], v[110:113]
	v_mfma_f32_16x16x128_f8f6f4 v[106:109], v[140:147], v[26:33], v[106:109]
	v_mfma_f32_16x16x128_f8f6f4 v[94:97], v[132:139], v[34:41], v[164:167]
	v_mfma_f32_16x16x128_f8f6f4 v[90:93], v[140:147], v[34:41], v[168:171]
	v_mfma_f32_16x16x128_f8f6f4 v[78:81], v[132:139], v[42:49], v[172:175]
	v_mfma_f32_16x16x128_f8f6f4 v[74:77], v[140:147], v[42:49], v[176:179]
	s_setprio 0
	s_barrier
	s_add_u32 s24, s4, 0x80
	ds_read_b128 v[26:29], v198 offset:49152
	ds_read_b128 v[30:33], v198 offset:50176
	ds_read_b128 v[148:151], v198 offset:51200
	ds_read_b128 v[152:155], v198 offset:52224
	ds_read_b128 v[156:159], v198 offset:53248
	ds_read_b128 v[160:163], v198 offset:54272
	ds_read_b128 v[164:167], v198 offset:55296
	ds_read_b128 v[168:171], v198 offset:56320
	s_addc_u32 s25, s5, 0
	s_add_i32 s46, s45, 0x18000
	s_mov_b32 m0, s46
	s_nop 0
	global_load_lds_dwordx4 v195, s[24:25]
	s_add_i32 s46, s45, 0x1a000
	s_mov_b32 m0, s46
	s_nop 0
	global_load_lds_dwordx4 v196, s[24:25]
	s_add_u32 s4, s4, 0x2080
	s_addc_u32 s5, s5, 0
	s_add_i32 s24, s45, 0x1c000
	s_mov_b32 m0, s24
	s_nop 0
	global_load_lds_dwordx4 v195, s[4:5]
	s_add_i32 s24, s45, 0x1e000
	s_mov_b32 m0, s24
	s_nop 0
	global_load_lds_dwordx4 v196, s[4:5]
	s_waitcnt vmcnt(6)
	s_waitcnt lgkmcnt(0)
	s_barrier
	s_setprio 1
	s_waitcnt lgkmcnt(6)
	v_mfma_f32_16x16x128_f8f6f4 v[54:57], v[2:9], v[26:33], v[54:57]
	v_mfma_f32_16x16x128_f8f6f4 v[50:53], v[10:17], v[26:33], v[50:53]
	s_waitcnt lgkmcnt(4)
	v_mfma_f32_16x16x128_f8f6f4 v[38:41], v[2:9], v[148:155], v[180:183]
	v_mfma_f32_16x16x128_f8f6f4 v[34:37], v[10:17], v[148:155], v[184:187]
	s_waitcnt lgkmcnt(2)
	v_mfma_f32_16x16x128_f8f6f4 v[22:25], v[2:9], v[156:163], v[202:205]
	v_mfma_f32_16x16x128_f8f6f4 v[18:21], v[10:17], v[156:163], v[206:209]
	s_waitcnt lgkmcnt(0)
	v_mfma_f32_16x16x128_f8f6f4 v[6:9], v[2:9], v[164:171], v[222:225]
	v_mfma_f32_16x16x128_f8f6f4 v[2:5], v[10:17], v[164:171], v[226:229]
	v_mfma_f32_16x16x128_f8f6f4 v[62:65], v[132:139], v[26:33], v[62:65]
	v_mfma_f32_16x16x128_f8f6f4 v[58:61], v[140:147], v[26:33], v[58:61]
	v_mfma_f32_16x16x128_f8f6f4 v[46:49], v[132:139], v[148:155], v[230:233]
	v_mfma_f32_16x16x128_f8f6f4 v[42:45], v[140:147], v[148:155], v[234:237]
	v_mfma_f32_16x16x128_f8f6f4 v[30:33], v[132:139], v[156:163], v[238:241]
	v_mfma_f32_16x16x128_f8f6f4 v[26:29], v[140:147], v[156:163], v[242:245]
	v_mfma_f32_16x16x128_f8f6f4 v[14:17], v[132:139], v[164:171], v[246:249]
	v_mfma_f32_16x16x128_f8f6f4 v[10:13], v[140:147], v[164:171], v[250:253]
	s_setprio 0
	s_barrier
	s_add_i32 s44, s44, 2
	s_add_u32 s42, s42, 0x100
	s_addc_u32 s43, s43, 0
	s_add_u32 s0, s0, 0x100
	s_addc_u32 s1, s1, 0
	s_cmp_gt_u32 s44, 5
	s_cbranch_scc0 .LBB0_641
.LBB0_644:
	v_cndmask_b32_e64 v131, 0, 1, s[12:13]
	v_cmp_ne_u32_e64 s[0:1], 1, v131
	s_andn2_b64 vcc, exec, s[12:13]
	s_cbranch_vccnz .LBB0_647
	s_add_i32 s2, s30, 2
	s_mul_i32 s2, s2, s92
	s_add_i32 s2, s2, s33
	s_cmpk_gt_i32 s2, 0x3ff
	s_mov_b64 s[12:13], 0
	s_cbranch_scc1 .LBB0_648
	s_lshl_b32 s3, s2, 7
	s_and_b32 s3, s3, 0x380
	s_ashr_i32 s2, s2, 3
	s_add_i32 s2, s3, s2
	s_ashr_i32 s3, s2, 31
	s_lshr_b32 s3, s3, 27
	s_add_i32 s3, s2, s3
	s_ashr_i32 s4, s3, 5
	s_andn2_b32 s3, s3, 31
	s_sub_i32 s2, s2, s3
	s_ashr_i32 s3, s2, 31
	s_lshr_b32 s3, s3, 29
	s_add_i32 s3, s2, s3
	s_ashr_i32 s7, s3, 3
	s_and_b32 s3, s3, -8
	s_lshl_b32 s4, s4, 3
	s_sub_i32 s2, s2, s3
	s_add_i32 s14, s2, s4
	s_mov_b64 s[12:13], -1
	s_branch .LBB0_648

; #define PG8_BAR __builtin_amdgcn_s_barrier()
; template <class Epi, class Sched, bool F8 = false, bool PF = false, bool I8 = false, int PID = -1>
; __device__ __forceinline__ void gemm_phase(LAS unsigned char* lds, LAS unsigned char* xlds, const int RP, const int RPB, const int nt, const Sched& S, const Epi& E, const int stagger_ticks) {
;     ...
;         if (wr == 0) PG8_BAR;
.LBB0_648:
	s_and_b64 vcc, exec, s[22:23]
	s_cbranch_vccz .Lmy_nobar4
	s_barrier

; #define PG8_STAGE(bufoff, gbase, voff) do { PG8_GLDS((const char*)(gbase), (voff)[0], ldsb + (bufoff)); PG8_GLDS((const char*)(gbase), (voff)[1], ldsb + (bufoff) + 8192u); } while (0)
; #define PG8_STAGEA(bufoff, gbase, o0, o1) do { PG8_GLDS((const char*)(gbase), (o0), ldsb + (bufoff)); PG8_GLDS((const char*)(gbase), (o1), ldsb + (bufoff) + 8192u); } while (0)
; #define PG8_STAGEA1(bufoff, gbase) do { if constexpr (Sched::GATHER) { PG8_STAGEA(bufoff, gbase, vA2, vA3); } else { PG8_STAGEA(bufoff, (gbase) + hstep, vA0, vA1); } } while (0)
; #define PG8_LDA(dst, b, h) do { if constexpr (F8) { _Pragma("unroll") for (int m = 0; m < 4; ++m) dst##8[m] = PG8_LD32(lds + PG8_SA(b, h) + aoff + m * 2048); } else { \
;         _Pragma("unroll") for (int m = 0; m < 4; ++m) _Pragma("unroll") for (int k = 0; k < 2; ++k) dst[m][k] = *(const LAS bf16x8*)(lds + PG8_SA(b, h) + aoff + m * 2048 + k * 1024); } } while (0)
; #define PG8_LDB(dst, b, h) do { if constexpr (F8) { _Pragma("unroll") for (int n = 0; n < 2; ++n) dst##8[n] = PG8_LD32(lds + PG8_SB(b, h) + boff + n * 2048); } else { \
;         _Pragma("unroll") for (int n = 0; n < 2; ++n) _Pragma("unroll") for (int k = 0; k < 2; ++k) dst[n][k] = *(const LAS bf16x8*)(lds + PG8_SB(b, h) + boff + n * 2048 + k * 1024); } } while (0)
; template <class Epi, class Sched, bool F8 = false, bool PF = false, bool I8 = false, int PID = -1>
; __device__ __forceinline__ void gemm_phase(LAS unsigned char* lds, LAS unsigned char* xlds, const int RP, const int RPB, const int nt, const Sched& S, const Epi& E, const int stagger_ticks) {
;     ...
;             PG8_LDB(B0, 0, 0); PG8_LDB(B1, 0, 1); PG8_SCHED; PG8_LDA(At, 0, 0); PG8_STAGEA1(PG8_SA(1, 1), a1);
;             if (Sched::GATHER) { if (last) { const u32x4 nv = *nslot; vA0 = nv.x; vA1 = nv.y; vA2 = nv.z; vA3 = nv.w; } }
;             PG8_WAIT_VX(); PG8_WAIT_L(0); PG8_BAR; PG8_MMA(0, 0, At, B0); PG8_MMA(0, 1, At, B1); PG8_BAR; PG8_SCHED;
;             if constexpr (Epi::BIAS_DMA) { if (t == 0 && has_next) E.bias_dma(nxt, xlds + 8192 + ((ui + 1) & 1) * Epi::BIAS_STRIDE, wid, lane); }
;             PG8_LDA(At, 0, 1); PG8_STAGE(PG8_SB(0, 0), b2, voffB); PG8_STAGE(PG8_SB(0, 1), b2 + hstepB, voffB); PG8_STAGEA(PG8_SA(0, 0), a2, vA0, vA1);
;             PG8_WAIT_VX(); PG8_WAIT_L(0); PG8_BAR; PG8_MMA(1, 0, At, B0); PG8_MMA(1, 1, At, B1); PG8_BAR; PG8_SCHED;
.LBB0_753:
	s_mov_b32 s46, s38
	s_add_u32 s100, s0, 0xfffe0000
	s_addc_u32 s101, s1, -1
	s_add_i32 s47, s46, 0x8000
	s_mov_b32 m0, s47
	s_nop 0
	global_load_lds_dwordx4 v1, s[100:101]
	s_add_i32 s47, s46, 0xa000
	s_mov_b32 m0, s47
	s_nop 0
	global_load_lds_dwordx4 v174, s[100:101]
	v_add_u32_e32 v142, 0x10000, v177
	v_add_u32_e32 v155, 0x14000, v177
	ds_read_b128 v[130:133], v142
	ds_read_b128 v[134:137], v142 offset:1024
	ds_read_b128 v[138:141], v142 offset:2048
	ds_read_b128 v[142:145], v142 offset:3072
	ds_read_b128 v[146:149], v155
	ds_read_b128 v[150:153], v155 offset:1024
	ds_read_b128 v[156:159], v155 offset:2048
	ds_read_b128 v[160:163], v155 offset:3072
	s_add_u32 s2, s0, 0xfffe0080
	s_addc_u32 s3, s1, -1
	s_cmp_eq_u32 s45, 4
	s_cselect_b32 s30, s6, s2
	s_cselect_b32 s31, s7, s3
	s_cselect_b32 s28, s8, s43
	s_cselect_b32 s29, s9, s44
	s_add_u32 s2, s30, 0x80
	s_addc_u32 s3, s31, 0
	ds_read_b128 v[164:167], v178
	ds_read_b128 v[168:171], v178 offset:1024
	ds_read_b128 v[180:183], v178 offset:2048
	ds_read_b128 v[184:187], v178 offset:3072
	ds_read_b128 v[188:191], v178 offset:4096
	ds_read_b128 v[192:195], v178 offset:5120
	ds_read_b128 v[196:199], v178 offset:6144
	ds_read_b128 v[200:203], v178 offset:7168
	s_add_i32 s47, s46, 0xc000
	s_mov_b32 m0, s47
	s_nop 0
	global_load_lds_dwordx4 v1, s[0:1]
	s_add_i32 s47, s46, 0xe000
	s_mov_b32 m0, s47
	s_nop 0
	global_load_lds_dwordx4 v174, s[0:1]
	s_waitcnt vmcnt(8)
	s_waitcnt lgkmcnt(0)
	s_barrier
	s_setprio 1
	s_waitcnt lgkmcnt(6)
	v_mfma_f32_16x16x128_f8f6f4 v[114:117], v[130:137], v[164:171], v[114:117]
	v_mfma_f32_16x16x128_f8f6f4 v[118:121], v[138:145], v[164:171], v[118:121]
	s_waitcnt lgkmcnt(4)
	v_mfma_f32_16x16x128_f8f6f4 v[110:113], v[130:137], v[180:187], v[110:113]
	v_mfma_f32_16x16x128_f8f6f4 v[106:109], v[138:145], v[180:187], v[106:109]
	s_waitcnt lgkmcnt(2)
	v_mfma_f32_16x16x128_f8f6f4 v[204:207], v[130:137], v[188:195], v[94:97]
	v_mfma_f32_16x16x128_f8f6f4 v[208:211], v[138:145], v[188:195], v[90:93]
	s_waitcnt lgkmcnt(0)
	v_mfma_f32_16x16x128_f8f6f4 v[212:215], v[130:137], v[196:203], v[78:81]
	v_mfma_f32_16x16x128_f8f6f4 v[216:219], v[138:145], v[196:203], v[74:77]
	v_mfma_f32_16x16x128_f8f6f4 v[122:125], v[146:153], v[164:171], v[122:125]
	v_mfma_f32_16x16x128_f8f6f4 v[126:129], v[156:163], v[164:171], v[126:129]
	v_mfma_f32_16x16x128_f8f6f4 v[102:105], v[146:153], v[180:187], v[102:105]
	v_mfma_f32_16x16x128_f8f6f4 v[98:101], v[156:163], v[180:187], v[98:101]
	v_mfma_f32_16x16x128_f8f6f4 v[164:167], v[146:153], v[188:195], v[86:89]
	v_mfma_f32_16x16x128_f8f6f4 v[168:171], v[156:163], v[188:195], v[82:85]
	v_mfma_f32_16x16x128_f8f6f4 v[180:183], v[146:153], v[196:203], v[70:73]
	v_mfma_f32_16x16x128_f8f6f4 v[184:187], v[156:163], v[196:203], v[66:69]
	s_setprio 0
	s_barrier
	s_nop 4
	ds_read_b128 v[66:69], v178 offset:16384
	ds_read_b128 v[70:73], v178 offset:17408
	ds_read_b128 v[74:77], v178 offset:18432
	ds_read_b128 v[78:81], v178 offset:19456
	ds_read_b128 v[82:85], v178 offset:20480
	ds_read_b128 v[86:89], v178 offset:21504
	ds_read_b128 v[90:93], v178 offset:22528
	ds_read_b128 v[94:97], v178 offset:23552
	s_add_i32 s47, s46, 0x10000
	s_mov_b32 m0, s47
	s_nop 0
	global_load_lds_dwordx4 v175, s[28:29]
	s_add_i32 s47, s46, 0x12000
	s_mov_b32 m0, s47
	s_nop 0
	global_load_lds_dwordx4 v176, s[28:29]
	s_add_u32 s48, s28, 0x2000
	s_addc_u32 s49, s29, 0
	s_add_i32 s47, s46, 0x14000
	s_mov_b32 m0, s47
	s_nop 0
	global_load_lds_dwordx4 v175, s[48:49]
	s_add_i32 s47, s46, 0x16000
	s_mov_b32 m0, s47
	s_nop 0
	global_load_lds_dwordx4 v176, s[48:49]
	s_waitcnt vmcnt(6)
	s_waitcnt lgkmcnt(0)
	s_barrier
	s_setprio 1
	s_waitcnt lgkmcnt(6)
	v_mfma_f32_16x16x128_f8f6f4 v[62:65], v[130:137], v[66:73], v[62:65]
	v_mfma_f32_16x16x128_f8f6f4 v[58:61], v[138:145], v[66:73], v[58:61]
	s_waitcnt lgkmcnt(4)
	v_mfma_f32_16x16x128_f8f6f4 v[188:191], v[130:137], v[74:81], v[46:49]
	v_mfma_f32_16x16x128_f8f6f4 v[192:195], v[138:145], v[74:81], v[42:45]
	s_waitcnt lgkmcnt(2)
	v_mfma_f32_16x16x128_f8f6f4 v[196:199], v[130:137], v[82:89], v[30:33]
	v_mfma_f32_16x16x128_f8f6f4 v[200:203], v[138:145], v[82:89], v[26:29]
	s_waitcnt lgkmcnt(0)
	v_mfma_f32_16x16x128_f8f6f4 v[220:223], v[130:137], v[90:97], v[14:17]
	v_mfma_f32_16x16x128_f8f6f4 v[224:227], v[138:145], v[90:97], v[10:13]
	v_mfma_f32_16x16x128_f8f6f4 v[54:57], v[146:153], v[66:73], v[54:57]
	v_mfma_f32_16x16x128_f8f6f4 v[50:53], v[156:163], v[66:73], v[50:53]
	v_mfma_f32_16x16x128_f8f6f4 v[228:231], v[146:153], v[74:81], v[38:41]
	v_mfma_f32_16x16x128_f8f6f4 v[232:235], v[156:163], v[74:81], v[34:37]
	v_mfma_f32_16x16x128_f8f6f4 v[236:239], v[146:153], v[82:89], v[22:25]
	v_mfma_f32_16x16x128_f8f6f4 v[240:243], v[156:163], v[82:89], v[18:21]
	v_mfma_f32_16x16x128_f8f6f4 v[244:247], v[146:153], v[90:97], v[6:9]
	v_mfma_f32_16x16x128_f8f6f4 v[248:251], v[156:163], v[90:97], v[2:5]
	s_setprio 0
	s_barrier
; #define PG8_STAGE(bufoff, gbase, voff) do { PG8_GLDS((const char*)(gbase), (voff)[0], ldsb + (bufoff)); PG8_GLDS((const char*)(gbase), (voff)[1], ldsb + (bufoff) + 8192u); } while (0)
; #define PG8_STAGEA(bufoff, gbase, o0, o1) do { PG8_GLDS((const char*)(gbase), (o0), ldsb + (bufoff)); PG8_GLDS((const char*)(gbase), (o1), ldsb + (bufoff) + 8192u); } while (0)
; #define PG8_STAGEA1(bufoff, gbase) do { if constexpr (Sched::GATHER) { PG8_STAGEA(bufoff, gbase, vA2, vA3); } else { PG8_STAGEA(bufoff, (gbase) + hstep, vA0, vA1); } } while (0)
; #define PG8_WAIT_VR() PG8_WAIT_V(8)
; #define PG8_WAIT_L(n) asm volatile("s_waitcnt lgkmcnt(" #n ")" ::: "memory")
; #define PG8_BAR __builtin_amdgcn_s_barrier()
; #define PG8_SCHED __builtin_amdgcn_sched_barrier(0)
;     const int nwg = nM * NN; int wgid = L;
;     { const int q = nwg >> 3, r = nwg & 7, xcd = wgid & 7, off = wgid >> 3; wgid = (xcd < r ? xcd * (q + 1) : r * (q + 1) + (xcd - r) * q) + off; }
;     constexpr int nig = WGM * NN; const int gid = wgid / nig, idx = wgid - gid * nig, fm = gid * WGM, left = nM - fm;
;     if (left >= WGM) { pm = fm + (idx % WGM); pn = idx / WGM; } else { pm = fm + (idx % left); pn = idx / left; }
; }
; template <class Epi, class Sched, bool F8 = false, bool PF = false, bool I8 = false, int PID = -1>
; __device__ __forceinline__ void gemm_phase(LAS unsigned char* lds, LAS unsigned char* xlds, const int RP, const int RPB, const int nt, const Sched& S, const Epi& E, const int stagger_ticks) {
;     ...
;             PG8_LDB(B0, 1, 0); PG8_LDB(B1, 1, 1); PG8_SCHED; PG8_LDA(At, 1, 0); PG8_STAGEA1(PG8_SA(0, 1), a2);
;             PG8_WAIT_VR(); PG8_WAIT_L(0); PG8_BAR; PG8_MMA(0, 0, At, B0); PG8_MMA(0, 1, At, B1); PG8_BAR; PG8_SCHED;
;             PG8_LDA(At, 1, 1); PG8_STAGE(PG8_SB(1, 0), b3, voffB); PG8_STAGE(PG8_SB(1, 1), b3 + hstepB, voffB); PG8_STAGEA(PG8_SA(1, 0), a3, vA0, vA1);
;             PG8_WAIT_VR(); PG8_WAIT_L(0); PG8_BAR; PG8_MMA(1, 0, At, B0); PG8_MMA(1, 1, At, B1); PG8_BAR; PG8_SCHED;
;         }
;         PROF_END(1); PROF_BEGIN(3);
;         if (wr == 0) PG8_BAR;
;         Unit nn; bool has_nn = false; unsigned gv[4] = {vA0, vA1, vA2, vA3};
;         if (has_next) { has_nn = S.next(ui + 2, nn); if (Sched::GATHER) { if (has_nn) S.a_offsets(nn, Rr, Cc, RP, gv); } }
	s_add_i32 s47, s46, 0x2000
	s_mov_b32 m0, s46
	s_nop 0
	global_load_lds_dwordx4 v1, s[30:31]
	s_nop 0
	s_mov_b32 m0, s47
	s_nop 0
	global_load_lds_dwordx4 v174, s[30:31]
	v_add_u32_e32 v10, 0x18000, v177
	s_nop 3
	ds_read_b128 v[2:5], v10
	ds_read_b128 v[6:9], v10 offset:1024
	ds_read_b128 v[18:21], v10 offset:2048
	ds_read_b128 v[22:25], v10 offset:3072
	v_add_u32_e32 v10, 0x1c000, v177
	ds_read_b128 v[130:133], v10
	ds_read_b128 v[134:137], v10 offset:1024
	ds_read_b128 v[138:141], v10 offset:2048
	ds_read_b128 v[142:145], v10 offset:3072
	ds_read_b128 v[10:13], v178 offset:32768
	ds_read_b128 v[14:17], v178 offset:33792
	ds_read_b128 v[26:29], v178 offset:34816
	ds_read_b128 v[30:33], v178 offset:35840
	ds_read_b128 v[34:37], v178 offset:36864
	ds_read_b128 v[38:41], v178 offset:37888
	ds_read_b128 v[42:45], v178 offset:38912
	ds_read_b128 v[46:49], v178 offset:39936
	s_add_u32 s30, s30, 0x20000
	s_addc_u32 s31, s31, 0
	s_add_i32 s47, s46, 0x4000
	s_mov_b32 m0, s47
	s_nop 0
	global_load_lds_dwordx4 v1, s[30:31]
	s_add_i32 s47, s46, 0x6000
	s_mov_b32 m0, s47
	s_nop 0
	global_load_lds_dwordx4 v174, s[30:31]
	s_waitcnt vmcnt(8)
	s_waitcnt lgkmcnt(0)
	s_barrier
	s_setprio 1
	s_waitcnt lgkmcnt(6)
	v_mfma_f32_16x16x128_f8f6f4 v[114:117], v[2:9], v[10:17], v[114:117]
	v_mfma_f32_16x16x128_f8f6f4 v[118:121], v[18:25], v[10:17], v[118:121]
	s_waitcnt lgkmcnt(4)
	v_mfma_f32_16x16x128_f8f6f4 v[110:113], v[2:9], v[26:33], v[110:113]
	v_mfma_f32_16x16x128_f8f6f4 v[106:109], v[18:25], v[26:33], v[106:109]
	s_waitcnt lgkmcnt(2)
	v_mfma_f32_16x16x128_f8f6f4 v[94:97], v[2:9], v[34:41], v[204:207]
	v_mfma_f32_16x16x128_f8f6f4 v[90:93], v[18:25], v[34:41], v[208:211]
	s_waitcnt lgkmcnt(0)
	v_mfma_f32_16x16x128_f8f6f4 v[78:81], v[2:9], v[42:49], v[212:215]
	v_mfma_f32_16x16x128_f8f6f4 v[74:77], v[18:25], v[42:49], v[216:219]
	v_mfma_f32_16x16x128_f8f6f4 v[122:125], v[130:137], v[10:17], v[122:125]
	v_mfma_f32_16x16x128_f8f6f4 v[126:129], v[138:145], v[10:17], v[126:129]
	v_mfma_f32_16x16x128_f8f6f4 v[102:105], v[130:137], v[26:33], v[102:105]
	v_mfma_f32_16x16x128_f8f6f4 v[98:101], v[138:145], v[26:33], v[98:101]
	v_mfma_f32_16x16x128_f8f6f4 v[86:89], v[130:137], v[34:41], v[164:167]
	v_mfma_f32_16x16x128_f8f6f4 v[82:85], v[138:145], v[34:41], v[168:171]
	v_mfma_f32_16x16x128_f8f6f4 v[70:73], v[130:137], v[42:49], v[180:183]
	v_mfma_f32_16x16x128_f8f6f4 v[66:69], v[138:145], v[42:49], v[184:187]
	s_setprio 0
	s_barrier
	s_add_u32 s30, s28, 0x80
	ds_read_b128 v[34:37], v178 offset:49152
	ds_read_b128 v[38:41], v178 offset:50176
	ds_read_b128 v[146:149], v178 offset:51200
	ds_read_b128 v[150:153], v178 offset:52224
	ds_read_b128 v[156:159], v178 offset:53248
	ds_read_b128 v[160:163], v178 offset:54272
	ds_read_b128 v[164:167], v178 offset:55296
	ds_read_b128 v[168:171], v178 offset:56320
	s_addc_u32 s31, s29, 0
	s_add_i32 s47, s46, 0x18000
	s_mov_b32 m0, s47
	s_nop 0
	global_load_lds_dwordx4 v175, s[30:31]
	s_add_i32 s47, s46, 0x1a000
	s_mov_b32 m0, s47
	s_nop 0
	global_load_lds_dwordx4 v176, s[30:31]
	s_add_u32 s28, s28, 0x2080
	s_addc_u32 s29, s29, 0
	s_add_i32 s30, s46, 0x1c000
	s_mov_b32 m0, s30
	s_nop 0
	global_load_lds_dwordx4 v175, s[28:29]
	s_add_i32 s30, s46, 0x1e000
	s_mov_b32 m0, s30
	s_nop 0
	global_load_lds_dwordx4 v176, s[28:29]
	s_waitcnt vmcnt(6)
	s_waitcnt lgkmcnt(0)
	s_barrier
	s_setprio 1
	s_waitcnt lgkmcnt(6)
	v_mfma_f32_16x16x128_f8f6f4 v[62:65], v[2:9], v[34:41], v[62:65]
	v_mfma_f32_16x16x128_f8f6f4 v[58:61], v[18:25], v[34:41], v[58:61]
	s_waitcnt lgkmcnt(4)
	v_mfma_f32_16x16x128_f8f6f4 v[46:49], v[2:9], v[146:153], v[188:191]
	v_mfma_f32_16x16x128_f8f6f4 v[42:45], v[18:25], v[146:153], v[192:195]
	s_waitcnt lgkmcnt(2)
	v_mfma_f32_16x16x128_f8f6f4 v[30:33], v[2:9], v[156:163], v[196:199]
	v_mfma_f32_16x16x128_f8f6f4 v[26:29], v[18:25], v[156:163], v[200:203]
	s_waitcnt lgkmcnt(0)
	v_mfma_f32_16x16x128_f8f6f4 v[14:17], v[2:9], v[164:171], v[220:223]
	v_mfma_f32_16x16x128_f8f6f4 v[10:13], v[18:25], v[164:171], v[224:227]
	v_mfma_f32_16x16x128_f8f6f4 v[54:57], v[130:137], v[34:41], v[54:57]
	v_mfma_f32_16x16x128_f8f6f4 v[50:53], v[138:145], v[34:41], v[50:53]
	v_mfma_f32_16x16x128_f8f6f4 v[38:41], v[130:137], v[146:153], v[228:231]
	v_mfma_f32_16x16x128_f8f6f4 v[34:37], v[138:145], v[146:153], v[232:235]
	v_mfma_f32_16x16x128_f8f6f4 v[22:25], v[130:137], v[156:163], v[236:239]
	v_mfma_f32_16x16x128_f8f6f4 v[18:21], v[138:145], v[156:163], v[240:243]
	v_mfma_f32_16x16x128_f8f6f4 v[6:9], v[130:137], v[164:171], v[244:247]
	v_mfma_f32_16x16x128_f8f6f4 v[2:5], v[138:145], v[164:171], v[248:251]
	s_setprio 0
	s_barrier
	s_add_i32 s45, s45, 2
	s_add_u32 s43, s43, 0x100
	s_addc_u32 s44, s44, 0
	s_add_u32 s0, s0, 0x100
	s_addc_u32 s1, s1, 0
	s_cmp_gt_u32 s45, 5
	s_cbranch_scc0 .LBB0_753
.LBB0_756:
	v_cndmask_b32_e64 v130, 0, 1, s[10:11]
	v_cmp_ne_u32_e64 s[0:1], 1, v130
	s_andn2_b64 vcc, exec, s[10:11]
	s_cbranch_vccnz .LBB0_759
	s_add_i32 s2, s42, 2
	s_mul_i32 s2, s2, s92
	s_add_i32 s2, s2, s33
	s_cmpk_gt_i32 s2, 0x3ff
	s_mov_b64 s[10:11], 0
	s_cbranch_scc1 .LBB0_760
	s_lshl_b32 s3, s2, 7
	s_and_b32 s3, s3, 0x380
	s_ashr_i32 s2, s2, 3
	s_add_i32 s2, s3, s2
	s_ashr_i32 s3, s2, 31
	s_lshr_b32 s3, s3, 27
	s_add_i32 s3, s2, s3
	s_ashr_i32 s5, s3, 5
	s_andn2_b32 s3, s3, 31
	s_sub_i32 s2, s2, s3
	s_ashr_i32 s3, s2, 31
	s_lshr_b32 s3, s3, 29
	s_add_i32 s3, s2, s3
	s_lshl_b32 s10, s5, 3
	s_ashr_i32 s5, s3, 3
	s_and_b32 s3, s3, -8
	s_sub_i32 s2, s2, s3
	s_add_i32 s10, s10, s2
	s_sub_i32 s12, 0xff, s10
	s_mov_b64 s[10:11], -1
	s_branch .LBB0_760

; #define PG8_BAR __builtin_amdgcn_s_barrier()
; template <class Epi, class Sched, bool F8 = false, bool PF = false, bool I8 = false, int PID = -1>
; __device__ __forceinline__ void gemm_phase(LAS unsigned char* lds, LAS unsigned char* xlds, const int RP, const int RPB, const int nt, const Sched& S, const Epi& E, const int stagger_ticks) {
;     ...
;         if (wr == 0) PG8_BAR;
.LBB0_760:
	s_and_b64 vcc, exec, s[24:25]
	s_cbranch_vccz .Lmy_nobar5
	s_barrier
